# speedup vs baseline: 1.0127x; 1.0127x over previous
.Lp_top:
	s_setprio 2
	v_readfirstlane_b32 s34, v10
	s_cmp_lt_u32 s34, s62
	s_cselect_b32 s45, s64, s65
	s_cselect_b32 s46, 0, s62
	s_cselect_b32 s48, s62, s63
	s_sub_u32 s47, s34, s46
	s_cmp_ge_u32 s47, s48
	s_cbranch_scc1 .Lp_done
	s_lshl_b32 s47, s47, 3
	s_add_u32 s45, s45, s47
	v_mov_b32_e32 v11, s45
	ds_read2_b32 v[12:13], v11 offset1:1
	s_waitcnt lgkmcnt(0)
	v_readfirstlane_b32 s35, v12
	v_readfirstlane_b32 s36, v13
	s_nop 1
	v_mov_b32_e32 v10, s35
	v_mov_b32_e32 v11, s36
	v_cndmask_b32_e64 v12, v10, v11, s[54:55]
	v_cndmask_b32_e64 v13, v10, v11, s[56:57]
	v_lshl_add_u32 v12, v12, 3, v61
	v_lshl_add_u32 v14, v13, 4, v62
	ds_read_b64 v[2:3], v12
	ds_read_b128 v[4:7], v14
	v_mad_u32_u24 v9, v13, s49, v58
	v_mov_b32_e32 v8, v56
	s_waitcnt lgkmcnt(0)
	v_add_u32_e32 v2, v2, v55
	v_and_b32_e32 v3, v3, v63
	s_nop 0
	v_readlane_b32 s41, v3, 0
	v_readlane_b32 s42, v3, 4
	s_max_u32 s43, s41, s42
	s_cmp_eq_u32 s43, 0
	s_cbranch_scc1 .Lp_zero
	ds_read_b64 v[36:37], v2
	v_cmp_gt_u32_e32 vcc, v3, v8
	v_add_u32_e32 v2, 64, v2
	v_add_u32_e32 v8, 16, v8
	v_mov_b32_e32 v33, 0x3c00
	s_waitcnt lgkmcnt(0)
	v_perm_b32 v32, v37, v36, v57
	v_cndmask_b32_e32 v33, 0, v33, vcc
	s_nop 0
	v_cndmask_b32_e32 v32, 0, v32, vcc
	s_nop 1
	v_mfma_f32_32x32x16_f16 v[96:111], v[32:35], v[64:67], 0
	v_mfma_f32_32x32x16_f16 v[112:127], v[32:35], v[68:71], 0
	s_nop 10
	s_mov_b32 s45, s43
	s_min_u32 s46, s45, 16
	s_cmp_eq_u32 s46, 16
	s_cbranch_scc1 .Lf16
	s_cmp_eq_u32 s46, 15
	s_cbranch_scc1 .Lf15
	s_cmp_eq_u32 s46, 14
	s_cbranch_scc1 .Lf14
	s_cmp_eq_u32 s46, 13
	s_cbranch_scc1 .Lf13
	s_cmp_eq_u32 s46, 12
	s_cbranch_scc1 .Lf12
	s_cmp_eq_u32 s46, 11
	s_cbranch_scc1 .Lf11
	s_cmp_eq_u32 s46, 10
	s_cbranch_scc1 .Lf10
	s_cmp_eq_u32 s46, 9
	s_cbranch_scc1 .Lf9
	s_cmp_eq_u32 s46, 8
	s_cbranch_scc1 .Lf8
	s_cmp_eq_u32 s46, 7
	s_cbranch_scc1 .Lf7
	s_cmp_eq_u32 s46, 6
	s_cbranch_scc1 .Lf6
	s_cmp_eq_u32 s46, 5
	s_cbranch_scc1 .Lf5
	s_cmp_eq_u32 s46, 4
	s_cbranch_scc1 .Lf4
	s_cmp_eq_u32 s46, 3
	s_cbranch_scc1 .Lf3
	s_cmp_eq_u32 s46, 2
	s_cbranch_scc1 .Lf2
.Lf1:
	s_setprio 0
	v_add_f32_e64 v24, |v96|, 0
	s_nop 10
	v_mfma_f32_32x32x16_f16 v[96:111], v[32:35], v[72:75], 0
	v_add_f32_e64 v25, |v112|, 0
	s_nop 10
	v_mfma_f32_32x32x16_f16 v[112:127], v[32:35], v[76:79], 0
	v_add_f32_e64 v26, |v96|, 0
	s_nop 10
	v_mfma_f32_32x32x16_f16 v[96:111], v[32:35], v[80:83], 0
	v_add_f32_e64 v27, |v112|, 0
	s_nop 10
	v_mfma_f32_32x32x16_f16 v[112:127], v[32:35], v[84:87], 0
	v_add_f32_e64 v28, |v96|, 0
	s_nop 10
	v_mfma_f32_32x32x16_f16 v[96:111], v[32:35], v[88:91], 0
	v_add_f32_e64 v29, |v112|, 0
	s_nop 10
	v_mfma_f32_32x32x16_f16 v[112:127], v[32:35], v[92:95], 0
	v_add_f32_e64 v30, |v96|, 0
	s_nop 10
	v_add_f32_e64 v31, |v112|, 0
	s_nop 10
	s_branch .Lafter_first
.Lf2:
	s_setprio 0
	v_add_f32_e64 v24, |v96|, |v97|
	s_nop 10
	v_mfma_f32_32x32x16_f16 v[96:111], v[32:35], v[72:75], 0
	v_add_f32_e64 v25, |v112|, |v113|
	s_nop 10
	v_mfma_f32_32x32x16_f16 v[112:127], v[32:35], v[76:79], 0
	v_add_f32_e64 v26, |v96|, |v97|
	s_nop 10
	v_mfma_f32_32x32x16_f16 v[96:111], v[32:35], v[80:83], 0
	v_add_f32_e64 v27, |v112|, |v113|
	s_nop 10
	v_mfma_f32_32x32x16_f16 v[112:127], v[32:35], v[84:87], 0
	v_add_f32_e64 v28, |v96|, |v97|
	s_nop 10
	v_mfma_f32_32x32x16_f16 v[96:111], v[32:35], v[88:91], 0
	v_add_f32_e64 v29, |v112|, |v113|
	s_nop 10
	v_mfma_f32_32x32x16_f16 v[112:127], v[32:35], v[92:95], 0
	v_add_f32_e64 v30, |v96|, |v97|
	s_nop 10
	v_add_f32_e64 v31, |v112|, |v113|
	s_nop 10
	s_branch .Lafter_first
.Lf3:
	s_setprio 0
	v_add_f32_e64 v38, |v96|, |v97|
	v_add_f32_e64 v24, v38, |v98|
	s_nop 9
	v_mfma_f32_32x32x16_f16 v[96:111], v[32:35], v[72:75], 0
	v_add_f32_e64 v38, |v112|, |v113|
	v_add_f32_e64 v25, v38, |v114|
	s_nop 9
	v_mfma_f32_32x32x16_f16 v[112:127], v[32:35], v[76:79], 0
	v_add_f32_e64 v38, |v96|, |v97|
	v_add_f32_e64 v26, v38, |v98|
	s_nop 9
	v_mfma_f32_32x32x16_f16 v[96:111], v[32:35], v[80:83], 0
	v_add_f32_e64 v38, |v112|, |v113|
	v_add_f32_e64 v27, v38, |v114|
	s_nop 9
	v_mfma_f32_32x32x16_f16 v[112:127], v[32:35], v[84:87], 0
	v_add_f32_e64 v38, |v96|, |v97|
	v_add_f32_e64 v28, v38, |v98|
	s_nop 9
	v_mfma_f32_32x32x16_f16 v[96:111], v[32:35], v[88:91], 0
	v_add_f32_e64 v38, |v112|, |v113|
	v_add_f32_e64 v29, v38, |v114|
	s_nop 9
	v_mfma_f32_32x32x16_f16 v[112:127], v[32:35], v[92:95], 0
	v_add_f32_e64 v38, |v96|, |v97|
	v_add_f32_e64 v30, v38, |v98|
	s_nop 9
	v_add_f32_e64 v38, |v112|, |v113|
	v_add_f32_e64 v31, v38, |v114|
	s_nop 9
	s_branch .Lafter_first
.Lf4:
	s_setprio 0
	v_add_f32_e64 v38, |v96|, |v97|
	v_add_f32_e64 v39, |v98|, |v99|
	v_add_f32_e32 v24, v38, v39
	s_nop 8
	v_mfma_f32_32x32x16_f16 v[96:111], v[32:35], v[72:75], 0
	v_add_f32_e64 v38, |v112|, |v113|
	v_add_f32_e64 v39, |v114|, |v115|
	v_add_f32_e32 v25, v38, v39
	s_nop 8
	v_mfma_f32_32x32x16_f16 v[112:127], v[32:35], v[76:79], 0
	v_add_f32_e64 v38, |v96|, |v97|
	v_add_f32_e64 v39, |v98|, |v99|
	v_add_f32_e32 v26, v38, v39
	s_nop 8
	v_mfma_f32_32x32x16_f16 v[96:111], v[32:35], v[80:83], 0
	v_add_f32_e64 v38, |v112|, |v113|
	v_add_f32_e64 v39, |v114|, |v115|
	v_add_f32_e32 v27, v38, v39
	s_nop 8
	v_mfma_f32_32x32x16_f16 v[112:127], v[32:35], v[84:87], 0
	v_add_f32_e64 v38, |v96|, |v97|
	v_add_f32_e64 v39, |v98|, |v99|
	v_add_f32_e32 v28, v38, v39
	s_nop 8
	v_mfma_f32_32x32x16_f16 v[96:111], v[32:35], v[88:91], 0
	v_add_f32_e64 v38, |v112|, |v113|
	v_add_f32_e64 v39, |v114|, |v115|
	v_add_f32_e32 v29, v38, v39
	s_nop 8
	v_mfma_f32_32x32x16_f16 v[112:127], v[32:35], v[92:95], 0
	v_add_f32_e64 v38, |v96|, |v97|
	v_add_f32_e64 v39, |v98|, |v99|
	v_add_f32_e32 v30, v38, v39
	s_nop 8
	v_add_f32_e64 v38, |v112|, |v113|
	v_add_f32_e64 v39, |v114|, |v115|
	v_add_f32_e32 v31, v38, v39
	s_nop 8
	s_branch .Lafter_first
.Lf5:
	s_setprio 0
	v_add_f32_e64 v38, |v96|, |v97|
	v_add_f32_e64 v39, |v98|, |v99|
	v_add_f32_e64 v38, v38, |v100|
	v_add_f32_e32 v24, v38, v39
	s_nop 7
	v_mfma_f32_32x32x16_f16 v[96:111], v[32:35], v[72:75], 0
	v_add_f32_e64 v38, |v112|, |v113|
	v_add_f32_e64 v39, |v114|, |v115|
	v_add_f32_e64 v38, v38, |v116|
	v_add_f32_e32 v25, v38, v39
	s_nop 7
	v_mfma_f32_32x32x16_f16 v[112:127], v[32:35], v[76:79], 0
	v_add_f32_e64 v38, |v96|, |v97|
	v_add_f32_e64 v39, |v98|, |v99|
	v_add_f32_e64 v38, v38, |v100|
	v_add_f32_e32 v26, v38, v39
	s_nop 7
	v_mfma_f32_32x32x16_f16 v[96:111], v[32:35], v[80:83], 0
	v_add_f32_e64 v38, |v112|, |v113|
	v_add_f32_e64 v39, |v114|, |v115|
	v_add_f32_e64 v38, v38, |v116|
	v_add_f32_e32 v27, v38, v39
	s_nop 7
	v_mfma_f32_32x32x16_f16 v[112:127], v[32:35], v[84:87], 0
	v_add_f32_e64 v38, |v96|, |v97|
	v_add_f32_e64 v39, |v98|, |v99|
	v_add_f32_e64 v38, v38, |v100|
	v_add_f32_e32 v28, v38, v39
	s_nop 7
	v_mfma_f32_32x32x16_f16 v[96:111], v[32:35], v[88:91], 0
	v_add_f32_e64 v38, |v112|, |v113|
	v_add_f32_e64 v39, |v114|, |v115|
	v_add_f32_e64 v38, v38, |v116|
	v_add_f32_e32 v29, v38, v39
	s_nop 7
	v_mfma_f32_32x32x16_f16 v[112:127], v[32:35], v[92:95], 0
	v_add_f32_e64 v38, |v96|, |v97|
	v_add_f32_e64 v39, |v98|, |v99|
	v_add_f32_e64 v38, v38, |v100|
	v_add_f32_e32 v30, v38, v39
	s_nop 7
	v_add_f32_e64 v38, |v112|, |v113|
	v_add_f32_e64 v39, |v114|, |v115|
	v_add_f32_e64 v38, v38, |v116|
	v_add_f32_e32 v31, v38, v39
	s_nop 7
	s_branch .Lafter_first
.Lf6:
	s_setprio 0
	v_add_f32_e64 v38, |v96|, |v97|
	v_add_f32_e64 v39, |v98|, |v99|
	v_add_f32_e64 v38, v38, |v100|
	v_add_f32_e64 v39, v39, |v101|
	v_add_f32_e32 v24, v38, v39
	s_nop 6
	v_mfma_f32_32x32x16_f16 v[96:111], v[32:35], v[72:75], 0
	v_add_f32_e64 v38, |v112|, |v113|
	v_add_f32_e64 v39, |v114|, |v115|
	v_add_f32_e64 v38, v38, |v116|
	v_add_f32_e64 v39, v39, |v117|
	v_add_f32_e32 v25, v38, v39
	s_nop 6
	v_mfma_f32_32x32x16_f16 v[112:127], v[32:35], v[76:79], 0
	v_add_f32_e64 v38, |v96|, |v97|
	v_add_f32_e64 v39, |v98|, |v99|
	v_add_f32_e64 v38, v38, |v100|
	v_add_f32_e64 v39, v39, |v101|
	v_add_f32_e32 v26, v38, v39
	s_nop 6
	v_mfma_f32_32x32x16_f16 v[96:111], v[32:35], v[80:83], 0
	v_add_f32_e64 v38, |v112|, |v113|
	v_add_f32_e64 v39, |v114|, |v115|
	v_add_f32_e64 v38, v38, |v116|
	v_add_f32_e64 v39, v39, |v117|
	v_add_f32_e32 v27, v38, v39
	s_nop 6
	v_mfma_f32_32x32x16_f16 v[112:127], v[32:35], v[84:87], 0
	v_add_f32_e64 v38, |v96|, |v97|
	v_add_f32_e64 v39, |v98|, |v99|
	v_add_f32_e64 v38, v38, |v100|
	v_add_f32_e64 v39, v39, |v101|
	v_add_f32_e32 v28, v38, v39
	s_nop 6
	v_mfma_f32_32x32x16_f16 v[96:111], v[32:35], v[88:91], 0
	v_add_f32_e64 v38, |v112|, |v113|
	v_add_f32_e64 v39, |v114|, |v115|
	v_add_f32_e64 v38, v38, |v116|
	v_add_f32_e64 v39, v39, |v117|
	v_add_f32_e32 v29, v38, v39
	s_nop 6
	v_mfma_f32_32x32x16_f16 v[112:127], v[32:35], v[92:95], 0
	v_add_f32_e64 v38, |v96|, |v97|
	v_add_f32_e64 v39, |v98|, |v99|
	v_add_f32_e64 v38, v38, |v100|
	v_add_f32_e64 v39, v39, |v101|
	v_add_f32_e32 v30, v38, v39
	s_nop 6
	v_add_f32_e64 v38, |v112|, |v113|
	v_add_f32_e64 v39, |v114|, |v115|
	v_add_f32_e64 v38, v38, |v116|
	v_add_f32_e64 v39, v39, |v117|
	v_add_f32_e32 v31, v38, v39
	s_nop 6
	s_branch .Lafter_first
.Lf7:
	s_setprio 0
	v_add_f32_e64 v38, |v96|, |v97|
	v_add_f32_e64 v39, |v98|, |v99|
	v_add_f32_e64 v38, v38, |v100|
	v_add_f32_e64 v39, v39, |v101|
	v_add_f32_e64 v38, v38, |v102|
	v_add_f32_e32 v24, v38, v39
	s_nop 5
	v_mfma_f32_32x32x16_f16 v[96:111], v[32:35], v[72:75], 0
	v_add_f32_e64 v38, |v112|, |v113|
	v_add_f32_e64 v39, |v114|, |v115|
	v_add_f32_e64 v38, v38, |v116|
	v_add_f32_e64 v39, v39, |v117|
	v_add_f32_e64 v38, v38, |v118|
	v_add_f32_e32 v25, v38, v39
	s_nop 5
	v_mfma_f32_32x32x16_f16 v[112:127], v[32:35], v[76:79], 0
	v_add_f32_e64 v38, |v96|, |v97|
	v_add_f32_e64 v39, |v98|, |v99|
	v_add_f32_e64 v38, v38, |v100|
	v_add_f32_e64 v39, v39, |v101|
	v_add_f32_e64 v38, v38, |v102|
	v_add_f32_e32 v26, v38, v39
	s_nop 5
	v_mfma_f32_32x32x16_f16 v[96:111], v[32:35], v[80:83], 0
	v_add_f32_e64 v38, |v112|, |v113|
	v_add_f32_e64 v39, |v114|, |v115|
	v_add_f32_e64 v38, v38, |v116|
	v_add_f32_e64 v39, v39, |v117|
	v_add_f32_e64 v38, v38, |v118|
	v_add_f32_e32 v27, v38, v39
	s_nop 5
	v_mfma_f32_32x32x16_f16 v[112:127], v[32:35], v[84:87], 0
	v_add_f32_e64 v38, |v96|, |v97|
	v_add_f32_e64 v39, |v98|, |v99|
	v_add_f32_e64 v38, v38, |v100|
	v_add_f32_e64 v39, v39, |v101|
	v_add_f32_e64 v38, v38, |v102|
	v_add_f32_e32 v28, v38, v39
	s_nop 5
	v_mfma_f32_32x32x16_f16 v[96:111], v[32:35], v[88:91], 0
	v_add_f32_e64 v38, |v112|, |v113|
	v_add_f32_e64 v39, |v114|, |v115|
	v_add_f32_e64 v38, v38, |v116|
	v_add_f32_e64 v39, v39, |v117|
	v_add_f32_e64 v38, v38, |v118|
	v_add_f32_e32 v29, v38, v39
	s_nop 5
	v_mfma_f32_32x32x16_f16 v[112:127], v[32:35], v[92:95], 0
	v_add_f32_e64 v38, |v96|, |v97|
	v_add_f32_e64 v39, |v98|, |v99|
	v_add_f32_e64 v38, v38, |v100|
	v_add_f32_e64 v39, v39, |v101|
	v_add_f32_e64 v38, v38, |v102|
	v_add_f32_e32 v30, v38, v39
	s_nop 5
	v_add_f32_e64 v38, |v112|, |v113|
	v_add_f32_e64 v39, |v114|, |v115|
	v_add_f32_e64 v38, v38, |v116|
	v_add_f32_e64 v39, v39, |v117|
	v_add_f32_e64 v38, v38, |v118|
	v_add_f32_e32 v31, v38, v39
	s_nop 5
	s_branch .Lafter_first
.Lf8:
	s_setprio 0
	v_add_f32_e64 v38, |v96|, |v97|
	v_add_f32_e64 v39, |v98|, |v99|
	v_add_f32_e64 v38, v38, |v100|
	v_add_f32_e64 v39, v39, |v101|
	v_add_f32_e64 v38, v38, |v102|
	v_add_f32_e64 v39, v39, |v103|
	v_add_f32_e32 v24, v38, v39
	s_nop 4
	v_mfma_f32_32x32x16_f16 v[96:111], v[32:35], v[72:75], 0
	v_add_f32_e64 v38, |v112|, |v113|
	v_add_f32_e64 v39, |v114|, |v115|
	v_add_f32_e64 v38, v38, |v116|
	v_add_f32_e64 v39, v39, |v117|
	v_add_f32_e64 v38, v38, |v118|
	v_add_f32_e64 v39, v39, |v119|
	v_add_f32_e32 v25, v38, v39
	s_nop 4
	v_mfma_f32_32x32x16_f16 v[112:127], v[32:35], v[76:79], 0
	v_add_f32_e64 v38, |v96|, |v97|
	v_add_f32_e64 v39, |v98|, |v99|
	v_add_f32_e64 v38, v38, |v100|
	v_add_f32_e64 v39, v39, |v101|
	v_add_f32_e64 v38, v38, |v102|
	v_add_f32_e64 v39, v39, |v103|
	v_add_f32_e32 v26, v38, v39
	s_nop 4
	v_mfma_f32_32x32x16_f16 v[96:111], v[32:35], v[80:83], 0
	v_add_f32_e64 v38, |v112|, |v113|
	v_add_f32_e64 v39, |v114|, |v115|
	v_add_f32_e64 v38, v38, |v116|
	v_add_f32_e64 v39, v39, |v117|
	v_add_f32_e64 v38, v38, |v118|
	v_add_f32_e64 v39, v39, |v119|
	v_add_f32_e32 v27, v38, v39
	s_nop 4
	v_mfma_f32_32x32x16_f16 v[112:127], v[32:35], v[84:87], 0
	v_add_f32_e64 v38, |v96|, |v97|
	v_add_f32_e64 v39, |v98|, |v99|
	v_add_f32_e64 v38, v38, |v100|
	v_add_f32_e64 v39, v39, |v101|
	v_add_f32_e64 v38, v38, |v102|
	v_add_f32_e64 v39, v39, |v103|
	v_add_f32_e32 v28, v38, v39
	s_nop 4
	v_mfma_f32_32x32x16_f16 v[96:111], v[32:35], v[88:91], 0
	v_add_f32_e64 v38, |v112|, |v113|
	v_add_f32_e64 v39, |v114|, |v115|
	v_add_f32_e64 v38, v38, |v116|
	v_add_f32_e64 v39, v39, |v117|
	v_add_f32_e64 v38, v38, |v118|
	v_add_f32_e64 v39, v39, |v119|
	v_add_f32_e32 v29, v38, v39
	s_nop 4
	v_mfma_f32_32x32x16_f16 v[112:127], v[32:35], v[92:95], 0
	v_add_f32_e64 v38, |v96|, |v97|
	v_add_f32_e64 v39, |v98|, |v99|
	v_add_f32_e64 v38, v38, |v100|
	v_add_f32_e64 v39, v39, |v101|
	v_add_f32_e64 v38, v38, |v102|
	v_add_f32_e64 v39, v39, |v103|
	v_add_f32_e32 v30, v38, v39
	s_nop 4
	v_add_f32_e64 v38, |v112|, |v113|
	v_add_f32_e64 v39, |v114|, |v115|
	v_add_f32_e64 v38, v38, |v116|
	v_add_f32_e64 v39, v39, |v117|
	v_add_f32_e64 v38, v38, |v118|
	v_add_f32_e64 v39, v39, |v119|
	v_add_f32_e32 v31, v38, v39
	s_nop 4
	s_branch .Lafter_first
.Lf9:
	s_setprio 0
	v_add_f32_e64 v38, |v96|, |v97|
	v_add_f32_e64 v39, |v98|, |v99|
	v_add_f32_e64 v38, v38, |v100|
	v_add_f32_e64 v39, v39, |v101|
	v_add_f32_e64 v38, v38, |v102|
	v_add_f32_e64 v39, v39, |v103|
	v_add_f32_e64 v38, v38, |v104|
	v_add_f32_e32 v24, v38, v39
	s_nop 3
	v_mfma_f32_32x32x16_f16 v[96:111], v[32:35], v[72:75], 0
	v_add_f32_e64 v38, |v112|, |v113|
	v_add_f32_e64 v39, |v114|, |v115|
	v_add_f32_e64 v38, v38, |v116|
	v_add_f32_e64 v39, v39, |v117|
	v_add_f32_e64 v38, v38, |v118|
	v_add_f32_e64 v39, v39, |v119|
	v_add_f32_e64 v38, v38, |v120|
	v_add_f32_e32 v25, v38, v39
	s_nop 3
	v_mfma_f32_32x32x16_f16 v[112:127], v[32:35], v[76:79], 0
	v_add_f32_e64 v38, |v96|, |v97|
	v_add_f32_e64 v39, |v98|, |v99|
	v_add_f32_e64 v38, v38, |v100|
	v_add_f32_e64 v39, v39, |v101|
	v_add_f32_e64 v38, v38, |v102|
	v_add_f32_e64 v39, v39, |v103|
	v_add_f32_e64 v38, v38, |v104|
	v_add_f32_e32 v26, v38, v39
	s_nop 3
	v_mfma_f32_32x32x16_f16 v[96:111], v[32:35], v[80:83], 0
	v_add_f32_e64 v38, |v112|, |v113|
	v_add_f32_e64 v39, |v114|, |v115|
	v_add_f32_e64 v38, v38, |v116|
	v_add_f32_e64 v39, v39, |v117|
	v_add_f32_e64 v38, v38, |v118|
	v_add_f32_e64 v39, v39, |v119|
	v_add_f32_e64 v38, v38, |v120|
	v_add_f32_e32 v27, v38, v39
	s_nop 3
	v_mfma_f32_32x32x16_f16 v[112:127], v[32:35], v[84:87], 0
	v_add_f32_e64 v38, |v96|, |v97|
	v_add_f32_e64 v39, |v98|, |v99|
	v_add_f32_e64 v38, v38, |v100|
	v_add_f32_e64 v39, v39, |v101|
	v_add_f32_e64 v38, v38, |v102|
	v_add_f32_e64 v39, v39, |v103|
	v_add_f32_e64 v38, v38, |v104|
	v_add_f32_e32 v28, v38, v39
	s_nop 3
	v_mfma_f32_32x32x16_f16 v[96:111], v[32:35], v[88:91], 0
	v_add_f32_e64 v38, |v112|, |v113|
	v_add_f32_e64 v39, |v114|, |v115|
	v_add_f32_e64 v38, v38, |v116|
	v_add_f32_e64 v39, v39, |v117|
	v_add_f32_e64 v38, v38, |v118|
	v_add_f32_e64 v39, v39, |v119|
	v_add_f32_e64 v38, v38, |v120|
	v_add_f32_e32 v29, v38, v39
	s_nop 3
	v_mfma_f32_32x32x16_f16 v[112:127], v[32:35], v[92:95], 0
	v_add_f32_e64 v38, |v96|, |v97|
	v_add_f32_e64 v39, |v98|, |v99|
	v_add_f32_e64 v38, v38, |v100|
	v_add_f32_e64 v39, v39, |v101|
	v_add_f32_e64 v38, v38, |v102|
	v_add_f32_e64 v39, v39, |v103|
	v_add_f32_e64 v38, v38, |v104|
	v_add_f32_e32 v30, v38, v39
	s_nop 3
	v_add_f32_e64 v38, |v112|, |v113|
	v_add_f32_e64 v39, |v114|, |v115|
	v_add_f32_e64 v38, v38, |v116|
	v_add_f32_e64 v39, v39, |v117|
	v_add_f32_e64 v38, v38, |v118|
	v_add_f32_e64 v39, v39, |v119|
	v_add_f32_e64 v38, v38, |v120|
	v_add_f32_e32 v31, v38, v39
	s_nop 3
	s_branch .Lafter_first
.Lf10:
	s_setprio 0
	v_add_f32_e64 v38, |v96|, |v97|
	v_add_f32_e64 v39, |v98|, |v99|
	v_add_f32_e64 v38, v38, |v100|
	v_add_f32_e64 v39, v39, |v101|
	v_add_f32_e64 v38, v38, |v102|
	v_add_f32_e64 v39, v39, |v103|
	v_add_f32_e64 v38, v38, |v104|
	v_add_f32_e64 v39, v39, |v105|
	v_add_f32_e32 v24, v38, v39
	s_nop 2
	v_mfma_f32_32x32x16_f16 v[96:111], v[32:35], v[72:75], 0
	v_add_f32_e64 v38, |v112|, |v113|
	v_add_f32_e64 v39, |v114|, |v115|
	v_add_f32_e64 v38, v38, |v116|
	v_add_f32_e64 v39, v39, |v117|
	v_add_f32_e64 v38, v38, |v118|
	v_add_f32_e64 v39, v39, |v119|
	v_add_f32_e64 v38, v38, |v120|
	v_add_f32_e64 v39, v39, |v121|
	v_add_f32_e32 v25, v38, v39
	s_nop 2
	v_mfma_f32_32x32x16_f16 v[112:127], v[32:35], v[76:79], 0
	v_add_f32_e64 v38, |v96|, |v97|
	v_add_f32_e64 v39, |v98|, |v99|
	v_add_f32_e64 v38, v38, |v100|
	v_add_f32_e64 v39, v39, |v101|
	v_add_f32_e64 v38, v38, |v102|
	v_add_f32_e64 v39, v39, |v103|
	v_add_f32_e64 v38, v38, |v104|
	v_add_f32_e64 v39, v39, |v105|
	v_add_f32_e32 v26, v38, v39
	s_nop 2
	v_mfma_f32_32x32x16_f16 v[96:111], v[32:35], v[80:83], 0
	v_add_f32_e64 v38, |v112|, |v113|
	v_add_f32_e64 v39, |v114|, |v115|
	v_add_f32_e64 v38, v38, |v116|
	v_add_f32_e64 v39, v39, |v117|
	v_add_f32_e64 v38, v38, |v118|
	v_add_f32_e64 v39, v39, |v119|
	v_add_f32_e64 v38, v38, |v120|
	v_add_f32_e64 v39, v39, |v121|
	v_add_f32_e32 v27, v38, v39
	s_nop 2
	v_mfma_f32_32x32x16_f16 v[112:127], v[32:35], v[84:87], 0
	v_add_f32_e64 v38, |v96|, |v97|
	v_add_f32_e64 v39, |v98|, |v99|
	v_add_f32_e64 v38, v38, |v100|
	v_add_f32_e64 v39, v39, |v101|
	v_add_f32_e64 v38, v38, |v102|
	v_add_f32_e64 v39, v39, |v103|
	v_add_f32_e64 v38, v38, |v104|
	v_add_f32_e64 v39, v39, |v105|
	v_add_f32_e32 v28, v38, v39
	s_nop 2
	v_mfma_f32_32x32x16_f16 v[96:111], v[32:35], v[88:91], 0
	v_add_f32_e64 v38, |v112|, |v113|
	v_add_f32_e64 v39, |v114|, |v115|
	v_add_f32_e64 v38, v38, |v116|
	v_add_f32_e64 v39, v39, |v117|
	v_add_f32_e64 v38, v38, |v118|
	v_add_f32_e64 v39, v39, |v119|
	v_add_f32_e64 v38, v38, |v120|
	v_add_f32_e64 v39, v39, |v121|
	v_add_f32_e32 v29, v38, v39
	s_nop 2
	v_mfma_f32_32x32x16_f16 v[112:127], v[32:35], v[92:95], 0
	v_add_f32_e64 v38, |v96|, |v97|
	v_add_f32_e64 v39, |v98|, |v99|
	v_add_f32_e64 v38, v38, |v100|
	v_add_f32_e64 v39, v39, |v101|
	v_add_f32_e64 v38, v38, |v102|
	v_add_f32_e64 v39, v39, |v103|
	v_add_f32_e64 v38, v38, |v104|
	v_add_f32_e64 v39, v39, |v105|
	v_add_f32_e32 v30, v38, v39
	s_nop 2
	v_add_f32_e64 v38, |v112|, |v113|
	v_add_f32_e64 v39, |v114|, |v115|
	v_add_f32_e64 v38, v38, |v116|
	v_add_f32_e64 v39, v39, |v117|
	v_add_f32_e64 v38, v38, |v118|
	v_add_f32_e64 v39, v39, |v119|
	v_add_f32_e64 v38, v38, |v120|
	v_add_f32_e64 v39, v39, |v121|
	v_add_f32_e32 v31, v38, v39
	s_nop 2
	s_branch .Lafter_first
.Lf11:
	s_setprio 0
	v_add_f32_e64 v38, |v96|, |v97|
	v_add_f32_e64 v39, |v98|, |v99|
	v_add_f32_e64 v38, v38, |v100|
	v_add_f32_e64 v39, v39, |v101|
	v_add_f32_e64 v38, v38, |v102|
	v_add_f32_e64 v39, v39, |v103|
	v_add_f32_e64 v38, v38, |v104|
	v_add_f32_e64 v39, v39, |v105|
	v_add_f32_e64 v38, v38, |v106|
	v_add_f32_e32 v24, v38, v39
	s_nop 1
	v_mfma_f32_32x32x16_f16 v[96:111], v[32:35], v[72:75], 0
	v_add_f32_e64 v38, |v112|, |v113|
	v_add_f32_e64 v39, |v114|, |v115|
	v_add_f32_e64 v38, v38, |v116|
	v_add_f32_e64 v39, v39, |v117|
	v_add_f32_e64 v38, v38, |v118|
	v_add_f32_e64 v39, v39, |v119|
	v_add_f32_e64 v38, v38, |v120|
	v_add_f32_e64 v39, v39, |v121|
	v_add_f32_e64 v38, v38, |v122|
	v_add_f32_e32 v25, v38, v39
	s_nop 1
	v_mfma_f32_32x32x16_f16 v[112:127], v[32:35], v[76:79], 0
	v_add_f32_e64 v38, |v96|, |v97|
	v_add_f32_e64 v39, |v98|, |v99|
	v_add_f32_e64 v38, v38, |v100|
	v_add_f32_e64 v39, v39, |v101|
	v_add_f32_e64 v38, v38, |v102|
	v_add_f32_e64 v39, v39, |v103|
	v_add_f32_e64 v38, v38, |v104|
	v_add_f32_e64 v39, v39, |v105|
	v_add_f32_e64 v38, v38, |v106|
	v_add_f32_e32 v26, v38, v39
	s_nop 1
	v_mfma_f32_32x32x16_f16 v[96:111], v[32:35], v[80:83], 0
	v_add_f32_e64 v38, |v112|, |v113|
	v_add_f32_e64 v39, |v114|, |v115|
	v_add_f32_e64 v38, v38, |v116|
	v_add_f32_e64 v39, v39, |v117|
	v_add_f32_e64 v38, v38, |v118|
	v_add_f32_e64 v39, v39, |v119|
	v_add_f32_e64 v38, v38, |v120|
	v_add_f32_e64 v39, v39, |v121|
	v_add_f32_e64 v38, v38, |v122|
	v_add_f32_e32 v27, v38, v39
	s_nop 1
	v_mfma_f32_32x32x16_f16 v[112:127], v[32:35], v[84:87], 0
	v_add_f32_e64 v38, |v96|, |v97|
	v_add_f32_e64 v39, |v98|, |v99|
	v_add_f32_e64 v38, v38, |v100|
	v_add_f32_e64 v39, v39, |v101|
	v_add_f32_e64 v38, v38, |v102|
	v_add_f32_e64 v39, v39, |v103|
	v_add_f32_e64 v38, v38, |v104|
	v_add_f32_e64 v39, v39, |v105|
	v_add_f32_e64 v38, v38, |v106|
	v_add_f32_e32 v28, v38, v39
	s_nop 1
	v_mfma_f32_32x32x16_f16 v[96:111], v[32:35], v[88:91], 0
	v_add_f32_e64 v38, |v112|, |v113|
	v_add_f32_e64 v39, |v114|, |v115|
	v_add_f32_e64 v38, v38, |v116|
	v_add_f32_e64 v39, v39, |v117|
	v_add_f32_e64 v38, v38, |v118|
	v_add_f32_e64 v39, v39, |v119|
	v_add_f32_e64 v38, v38, |v120|
	v_add_f32_e64 v39, v39, |v121|
	v_add_f32_e64 v38, v38, |v122|
	v_add_f32_e32 v29, v38, v39
	s_nop 1
	v_mfma_f32_32x32x16_f16 v[112:127], v[32:35], v[92:95], 0
	v_add_f32_e64 v38, |v96|, |v97|
	v_add_f32_e64 v39, |v98|, |v99|
	v_add_f32_e64 v38, v38, |v100|
	v_add_f32_e64 v39, v39, |v101|
	v_add_f32_e64 v38, v38, |v102|
	v_add_f32_e64 v39, v39, |v103|
	v_add_f32_e64 v38, v38, |v104|
	v_add_f32_e64 v39, v39, |v105|
	v_add_f32_e64 v38, v38, |v106|
	v_add_f32_e32 v30, v38, v39
	s_nop 1
	v_add_f32_e64 v38, |v112|, |v113|
	v_add_f32_e64 v39, |v114|, |v115|
	v_add_f32_e64 v38, v38, |v116|
	v_add_f32_e64 v39, v39, |v117|
	v_add_f32_e64 v38, v38, |v118|
	v_add_f32_e64 v39, v39, |v119|
	v_add_f32_e64 v38, v38, |v120|
	v_add_f32_e64 v39, v39, |v121|
	v_add_f32_e64 v38, v38, |v122|
	v_add_f32_e32 v31, v38, v39
	s_nop 1
	s_branch .Lafter_first
.Lf12:
	s_setprio 0
	v_add_f32_e64 v38, |v96|, |v97|
	v_add_f32_e64 v39, |v98|, |v99|
	v_add_f32_e64 v38, v38, |v100|
	v_add_f32_e64 v39, v39, |v101|
	v_add_f32_e64 v38, v38, |v102|
	v_add_f32_e64 v39, v39, |v103|
	v_add_f32_e64 v38, v38, |v104|
	v_add_f32_e64 v39, v39, |v105|
	v_add_f32_e64 v38, v38, |v106|
	v_add_f32_e64 v39, v39, |v107|
	v_add_f32_e32 v24, v38, v39
	s_nop 0
	v_mfma_f32_32x32x16_f16 v[96:111], v[32:35], v[72:75], 0
	v_add_f32_e64 v38, |v112|, |v113|
	v_add_f32_e64 v39, |v114|, |v115|
	v_add_f32_e64 v38, v38, |v116|
	v_add_f32_e64 v39, v39, |v117|
	v_add_f32_e64 v38, v38, |v118|
	v_add_f32_e64 v39, v39, |v119|
	v_add_f32_e64 v38, v38, |v120|
	v_add_f32_e64 v39, v39, |v121|
	v_add_f32_e64 v38, v38, |v122|
	v_add_f32_e64 v39, v39, |v123|
	v_add_f32_e32 v25, v38, v39
	s_nop 0
	v_mfma_f32_32x32x16_f16 v[112:127], v[32:35], v[76:79], 0
	v_add_f32_e64 v38, |v96|, |v97|
	v_add_f32_e64 v39, |v98|, |v99|
	v_add_f32_e64 v38, v38, |v100|
	v_add_f32_e64 v39, v39, |v101|
	v_add_f32_e64 v38, v38, |v102|
	v_add_f32_e64 v39, v39, |v103|
	v_add_f32_e64 v38, v38, |v104|
	v_add_f32_e64 v39, v39, |v105|
	v_add_f32_e64 v38, v38, |v106|
	v_add_f32_e64 v39, v39, |v107|
	v_add_f32_e32 v26, v38, v39
	s_nop 0
	v_mfma_f32_32x32x16_f16 v[96:111], v[32:35], v[80:83], 0
	v_add_f32_e64 v38, |v112|, |v113|
	v_add_f32_e64 v39, |v114|, |v115|
	v_add_f32_e64 v38, v38, |v116|
	v_add_f32_e64 v39, v39, |v117|
	v_add_f32_e64 v38, v38, |v118|
	v_add_f32_e64 v39, v39, |v119|
	v_add_f32_e64 v38, v38, |v120|
	v_add_f32_e64 v39, v39, |v121|
	v_add_f32_e64 v38, v38, |v122|
	v_add_f32_e64 v39, v39, |v123|
	v_add_f32_e32 v27, v38, v39
	s_nop 0
	v_mfma_f32_32x32x16_f16 v[112:127], v[32:35], v[84:87], 0
	v_add_f32_e64 v38, |v96|, |v97|
	v_add_f32_e64 v39, |v98|, |v99|
	v_add_f32_e64 v38, v38, |v100|
	v_add_f32_e64 v39, v39, |v101|
	v_add_f32_e64 v38, v38, |v102|
	v_add_f32_e64 v39, v39, |v103|
	v_add_f32_e64 v38, v38, |v104|
	v_add_f32_e64 v39, v39, |v105|
	v_add_f32_e64 v38, v38, |v106|
	v_add_f32_e64 v39, v39, |v107|
	v_add_f32_e32 v28, v38, v39
	s_nop 0
	v_mfma_f32_32x32x16_f16 v[96:111], v[32:35], v[88:91], 0
	v_add_f32_e64 v38, |v112|, |v113|
	v_add_f32_e64 v39, |v114|, |v115|
	v_add_f32_e64 v38, v38, |v116|
	v_add_f32_e64 v39, v39, |v117|
	v_add_f32_e64 v38, v38, |v118|
	v_add_f32_e64 v39, v39, |v119|
	v_add_f32_e64 v38, v38, |v120|
	v_add_f32_e64 v39, v39, |v121|
	v_add_f32_e64 v38, v38, |v122|
	v_add_f32_e64 v39, v39, |v123|
	v_add_f32_e32 v29, v38, v39
	s_nop 0
	v_mfma_f32_32x32x16_f16 v[112:127], v[32:35], v[92:95], 0
	v_add_f32_e64 v38, |v96|, |v97|
	v_add_f32_e64 v39, |v98|, |v99|
	v_add_f32_e64 v38, v38, |v100|
	v_add_f32_e64 v39, v39, |v101|
	v_add_f32_e64 v38, v38, |v102|
	v_add_f32_e64 v39, v39, |v103|
	v_add_f32_e64 v38, v38, |v104|
	v_add_f32_e64 v39, v39, |v105|
	v_add_f32_e64 v38, v38, |v106|
	v_add_f32_e64 v39, v39, |v107|
	v_add_f32_e32 v30, v38, v39
	s_nop 0
	v_add_f32_e64 v38, |v112|, |v113|
	v_add_f32_e64 v39, |v114|, |v115|
	v_add_f32_e64 v38, v38, |v116|
	v_add_f32_e64 v39, v39, |v117|
	v_add_f32_e64 v38, v38, |v118|
	v_add_f32_e64 v39, v39, |v119|
	v_add_f32_e64 v38, v38, |v120|
	v_add_f32_e64 v39, v39, |v121|
	v_add_f32_e64 v38, v38, |v122|
	v_add_f32_e64 v39, v39, |v123|
	v_add_f32_e32 v31, v38, v39
	s_nop 0
	s_branch .Lafter_first
.Lf13:
	s_setprio 0
	v_add_f32_e64 v38, |v96|, |v97|
	v_add_f32_e64 v39, |v98|, |v99|
	v_add_f32_e64 v38, v38, |v100|
	v_add_f32_e64 v39, v39, |v101|
	v_add_f32_e64 v38, v38, |v102|
	v_add_f32_e64 v39, v39, |v103|
	v_add_f32_e64 v38, v38, |v104|
	v_add_f32_e64 v39, v39, |v105|
	v_add_f32_e64 v38, v38, |v106|
	v_add_f32_e64 v39, v39, |v107|
	v_add_f32_e64 v38, v38, |v108|
	v_add_f32_e32 v24, v38, v39
	v_mfma_f32_32x32x16_f16 v[96:111], v[32:35], v[72:75], 0
	v_add_f32_e64 v38, |v112|, |v113|
	v_add_f32_e64 v39, |v114|, |v115|
	v_add_f32_e64 v38, v38, |v116|
	v_add_f32_e64 v39, v39, |v117|
	v_add_f32_e64 v38, v38, |v118|
	v_add_f32_e64 v39, v39, |v119|
	v_add_f32_e64 v38, v38, |v120|
	v_add_f32_e64 v39, v39, |v121|
	v_add_f32_e64 v38, v38, |v122|
	v_add_f32_e64 v39, v39, |v123|
	v_add_f32_e64 v38, v38, |v124|
	v_add_f32_e32 v25, v38, v39
	v_mfma_f32_32x32x16_f16 v[112:127], v[32:35], v[76:79], 0
	v_add_f32_e64 v38, |v96|, |v97|
	v_add_f32_e64 v39, |v98|, |v99|
	v_add_f32_e64 v38, v38, |v100|
	v_add_f32_e64 v39, v39, |v101|
	v_add_f32_e64 v38, v38, |v102|
	v_add_f32_e64 v39, v39, |v103|
	v_add_f32_e64 v38, v38, |v104|
	v_add_f32_e64 v39, v39, |v105|
	v_add_f32_e64 v38, v38, |v106|
	v_add_f32_e64 v39, v39, |v107|
	v_add_f32_e64 v38, v38, |v108|
	v_add_f32_e32 v26, v38, v39
	v_mfma_f32_32x32x16_f16 v[96:111], v[32:35], v[80:83], 0
	v_add_f32_e64 v38, |v112|, |v113|
	v_add_f32_e64 v39, |v114|, |v115|
	v_add_f32_e64 v38, v38, |v116|
	v_add_f32_e64 v39, v39, |v117|
	v_add_f32_e64 v38, v38, |v118|
	v_add_f32_e64 v39, v39, |v119|
	v_add_f32_e64 v38, v38, |v120|
	v_add_f32_e64 v39, v39, |v121|
	v_add_f32_e64 v38, v38, |v122|
	v_add_f32_e64 v39, v39, |v123|
	v_add_f32_e64 v38, v38, |v124|
	v_add_f32_e32 v27, v38, v39
	v_mfma_f32_32x32x16_f16 v[112:127], v[32:35], v[84:87], 0
	v_add_f32_e64 v38, |v96|, |v97|
	v_add_f32_e64 v39, |v98|, |v99|
	v_add_f32_e64 v38, v38, |v100|
	v_add_f32_e64 v39, v39, |v101|
	v_add_f32_e64 v38, v38, |v102|
	v_add_f32_e64 v39, v39, |v103|
	v_add_f32_e64 v38, v38, |v104|
	v_add_f32_e64 v39, v39, |v105|
	v_add_f32_e64 v38, v38, |v106|
	v_add_f32_e64 v39, v39, |v107|
	v_add_f32_e64 v38, v38, |v108|
	v_add_f32_e32 v28, v38, v39
	v_mfma_f32_32x32x16_f16 v[96:111], v[32:35], v[88:91], 0
	v_add_f32_e64 v38, |v112|, |v113|
	v_add_f32_e64 v39, |v114|, |v115|
	v_add_f32_e64 v38, v38, |v116|
	v_add_f32_e64 v39, v39, |v117|
	v_add_f32_e64 v38, v38, |v118|
	v_add_f32_e64 v39, v39, |v119|
	v_add_f32_e64 v38, v38, |v120|
	v_add_f32_e64 v39, v39, |v121|
	v_add_f32_e64 v38, v38, |v122|
	v_add_f32_e64 v39, v39, |v123|
	v_add_f32_e64 v38, v38, |v124|
	v_add_f32_e32 v29, v38, v39
	v_mfma_f32_32x32x16_f16 v[112:127], v[32:35], v[92:95], 0
	v_add_f32_e64 v38, |v96|, |v97|
	v_add_f32_e64 v39, |v98|, |v99|
	v_add_f32_e64 v38, v38, |v100|
	v_add_f32_e64 v39, v39, |v101|
	v_add_f32_e64 v38, v38, |v102|
	v_add_f32_e64 v39, v39, |v103|
	v_add_f32_e64 v38, v38, |v104|
	v_add_f32_e64 v39, v39, |v105|
	v_add_f32_e64 v38, v38, |v106|
	v_add_f32_e64 v39, v39, |v107|
	v_add_f32_e64 v38, v38, |v108|
	v_add_f32_e32 v30, v38, v39
	v_add_f32_e64 v38, |v112|, |v113|
	v_add_f32_e64 v39, |v114|, |v115|
	v_add_f32_e64 v38, v38, |v116|
	v_add_f32_e64 v39, v39, |v117|
	v_add_f32_e64 v38, v38, |v118|
	v_add_f32_e64 v39, v39, |v119|
	v_add_f32_e64 v38, v38, |v120|
	v_add_f32_e64 v39, v39, |v121|
	v_add_f32_e64 v38, v38, |v122|
	v_add_f32_e64 v39, v39, |v123|
	v_add_f32_e64 v38, v38, |v124|
	v_add_f32_e32 v31, v38, v39
	s_branch .Lafter_first
.Lf14:
	s_setprio 0
	v_add_f32_e64 v38, |v96|, |v97|
	v_add_f32_e64 v39, |v98|, |v99|
	v_add_f32_e64 v38, v38, |v100|
	v_add_f32_e64 v39, v39, |v101|
	v_add_f32_e64 v38, v38, |v102|
	v_add_f32_e64 v39, v39, |v103|
	v_add_f32_e64 v38, v38, |v104|
	v_add_f32_e64 v39, v39, |v105|
	v_add_f32_e64 v38, v38, |v106|
	v_add_f32_e64 v39, v39, |v107|
	v_add_f32_e64 v38, v38, |v108|
	v_add_f32_e64 v39, v39, |v109|
	v_add_f32_e32 v24, v38, v39
	v_mfma_f32_32x32x16_f16 v[96:111], v[32:35], v[72:75], 0
	v_add_f32_e64 v38, |v112|, |v113|
	v_add_f32_e64 v39, |v114|, |v115|
	v_add_f32_e64 v38, v38, |v116|
	v_add_f32_e64 v39, v39, |v117|
	v_add_f32_e64 v38, v38, |v118|
	v_add_f32_e64 v39, v39, |v119|
	v_add_f32_e64 v38, v38, |v120|
	v_add_f32_e64 v39, v39, |v121|
	v_add_f32_e64 v38, v38, |v122|
	v_add_f32_e64 v39, v39, |v123|
	v_add_f32_e64 v38, v38, |v124|
	v_add_f32_e64 v39, v39, |v125|
	v_add_f32_e32 v25, v38, v39
	v_mfma_f32_32x32x16_f16 v[112:127], v[32:35], v[76:79], 0
	v_add_f32_e64 v38, |v96|, |v97|
	v_add_f32_e64 v39, |v98|, |v99|
	v_add_f32_e64 v38, v38, |v100|
	v_add_f32_e64 v39, v39, |v101|
	v_add_f32_e64 v38, v38, |v102|
	v_add_f32_e64 v39, v39, |v103|
	v_add_f32_e64 v38, v38, |v104|
	v_add_f32_e64 v39, v39, |v105|
	v_add_f32_e64 v38, v38, |v106|
	v_add_f32_e64 v39, v39, |v107|
	v_add_f32_e64 v38, v38, |v108|
	v_add_f32_e64 v39, v39, |v109|
	v_add_f32_e32 v26, v38, v39
	v_mfma_f32_32x32x16_f16 v[96:111], v[32:35], v[80:83], 0
	v_add_f32_e64 v38, |v112|, |v113|
	v_add_f32_e64 v39, |v114|, |v115|
	v_add_f32_e64 v38, v38, |v116|
	v_add_f32_e64 v39, v39, |v117|
	v_add_f32_e64 v38, v38, |v118|
	v_add_f32_e64 v39, v39, |v119|
	v_add_f32_e64 v38, v38, |v120|
	v_add_f32_e64 v39, v39, |v121|
	v_add_f32_e64 v38, v38, |v122|
	v_add_f32_e64 v39, v39, |v123|
	v_add_f32_e64 v38, v38, |v124|
	v_add_f32_e64 v39, v39, |v125|
	v_add_f32_e32 v27, v38, v39
	v_mfma_f32_32x32x16_f16 v[112:127], v[32:35], v[84:87], 0
	v_add_f32_e64 v38, |v96|, |v97|
	v_add_f32_e64 v39, |v98|, |v99|
	v_add_f32_e64 v38, v38, |v100|
	v_add_f32_e64 v39, v39, |v101|
	v_add_f32_e64 v38, v38, |v102|
	v_add_f32_e64 v39, v39, |v103|
	v_add_f32_e64 v38, v38, |v104|
	v_add_f32_e64 v39, v39, |v105|
	v_add_f32_e64 v38, v38, |v106|
	v_add_f32_e64 v39, v39, |v107|
	v_add_f32_e64 v38, v38, |v108|
	v_add_f32_e64 v39, v39, |v109|
	v_add_f32_e32 v28, v38, v39
	v_mfma_f32_32x32x16_f16 v[96:111], v[32:35], v[88:91], 0
	v_add_f32_e64 v38, |v112|, |v113|
	v_add_f32_e64 v39, |v114|, |v115|
	v_add_f32_e64 v38, v38, |v116|
	v_add_f32_e64 v39, v39, |v117|
	v_add_f32_e64 v38, v38, |v118|
	v_add_f32_e64 v39, v39, |v119|
	v_add_f32_e64 v38, v38, |v120|
	v_add_f32_e64 v39, v39, |v121|
	v_add_f32_e64 v38, v38, |v122|
	v_add_f32_e64 v39, v39, |v123|
	v_add_f32_e64 v38, v38, |v124|
	v_add_f32_e64 v39, v39, |v125|
	v_add_f32_e32 v29, v38, v39
	v_mfma_f32_32x32x16_f16 v[112:127], v[32:35], v[92:95], 0
	v_add_f32_e64 v38, |v96|, |v97|
	v_add_f32_e64 v39, |v98|, |v99|
	v_add_f32_e64 v38, v38, |v100|
	v_add_f32_e64 v39, v39, |v101|
	v_add_f32_e64 v38, v38, |v102|
	v_add_f32_e64 v39, v39, |v103|
	v_add_f32_e64 v38, v38, |v104|
	v_add_f32_e64 v39, v39, |v105|
	v_add_f32_e64 v38, v38, |v106|
	v_add_f32_e64 v39, v39, |v107|
	v_add_f32_e64 v38, v38, |v108|
	v_add_f32_e64 v39, v39, |v109|
	v_add_f32_e32 v30, v38, v39
	v_add_f32_e64 v38, |v112|, |v113|
	v_add_f32_e64 v39, |v114|, |v115|
	v_add_f32_e64 v38, v38, |v116|
	v_add_f32_e64 v39, v39, |v117|
	v_add_f32_e64 v38, v38, |v118|
	v_add_f32_e64 v39, v39, |v119|
	v_add_f32_e64 v38, v38, |v120|
	v_add_f32_e64 v39, v39, |v121|
	v_add_f32_e64 v38, v38, |v122|
	v_add_f32_e64 v39, v39, |v123|
	v_add_f32_e64 v38, v38, |v124|
	v_add_f32_e64 v39, v39, |v125|
	v_add_f32_e32 v31, v38, v39
	s_branch .Lafter_first
.Lf15:
	s_setprio 0
	v_add_f32_e64 v38, |v96|, |v97|
	v_add_f32_e64 v39, |v98|, |v99|
	v_add_f32_e64 v38, v38, |v100|
	v_add_f32_e64 v39, v39, |v101|
	v_add_f32_e64 v38, v38, |v102|
	v_add_f32_e64 v39, v39, |v103|
	v_add_f32_e64 v38, v38, |v104|
	v_add_f32_e64 v39, v39, |v105|
	v_add_f32_e64 v38, v38, |v106|
	v_add_f32_e64 v39, v39, |v107|
	v_add_f32_e64 v38, v38, |v108|
	v_add_f32_e64 v39, v39, |v109|
	v_add_f32_e64 v38, v38, |v110|
	v_add_f32_e32 v24, v38, v39
	v_mfma_f32_32x32x16_f16 v[96:111], v[32:35], v[72:75], 0
	v_add_f32_e64 v38, |v112|, |v113|
	v_add_f32_e64 v39, |v114|, |v115|
	v_add_f32_e64 v38, v38, |v116|
	v_add_f32_e64 v39, v39, |v117|
	v_add_f32_e64 v38, v38, |v118|
	v_add_f32_e64 v39, v39, |v119|
	v_add_f32_e64 v38, v38, |v120|
	v_add_f32_e64 v39, v39, |v121|
	v_add_f32_e64 v38, v38, |v122|
	v_add_f32_e64 v39, v39, |v123|
	v_add_f32_e64 v38, v38, |v124|
	v_add_f32_e64 v39, v39, |v125|
	v_add_f32_e64 v38, v38, |v126|
	v_add_f32_e32 v25, v38, v39
	v_mfma_f32_32x32x16_f16 v[112:127], v[32:35], v[76:79], 0
	v_add_f32_e64 v38, |v96|, |v97|
	v_add_f32_e64 v39, |v98|, |v99|
	v_add_f32_e64 v38, v38, |v100|
	v_add_f32_e64 v39, v39, |v101|
	v_add_f32_e64 v38, v38, |v102|
	v_add_f32_e64 v39, v39, |v103|
	v_add_f32_e64 v38, v38, |v104|
	v_add_f32_e64 v39, v39, |v105|
	v_add_f32_e64 v38, v38, |v106|
	v_add_f32_e64 v39, v39, |v107|
	v_add_f32_e64 v38, v38, |v108|
	v_add_f32_e64 v39, v39, |v109|
	v_add_f32_e64 v38, v38, |v110|
	v_add_f32_e32 v26, v38, v39
	v_mfma_f32_32x32x16_f16 v[96:111], v[32:35], v[80:83], 0
	v_add_f32_e64 v38, |v112|, |v113|
	v_add_f32_e64 v39, |v114|, |v115|
	v_add_f32_e64 v38, v38, |v116|
	v_add_f32_e64 v39, v39, |v117|
	v_add_f32_e64 v38, v38, |v118|
	v_add_f32_e64 v39, v39, |v119|
	v_add_f32_e64 v38, v38, |v120|
	v_add_f32_e64 v39, v39, |v121|
	v_add_f32_e64 v38, v38, |v122|
	v_add_f32_e64 v39, v39, |v123|
	v_add_f32_e64 v38, v38, |v124|
	v_add_f32_e64 v39, v39, |v125|
	v_add_f32_e64 v38, v38, |v126|
	v_add_f32_e32 v27, v38, v39
	v_mfma_f32_32x32x16_f16 v[112:127], v[32:35], v[84:87], 0
	v_add_f32_e64 v38, |v96|, |v97|
	v_add_f32_e64 v39, |v98|, |v99|
	v_add_f32_e64 v38, v38, |v100|
	v_add_f32_e64 v39, v39, |v101|
	v_add_f32_e64 v38, v38, |v102|
	v_add_f32_e64 v39, v39, |v103|
	v_add_f32_e64 v38, v38, |v104|
	v_add_f32_e64 v39, v39, |v105|
	v_add_f32_e64 v38, v38, |v106|
	v_add_f32_e64 v39, v39, |v107|
	v_add_f32_e64 v38, v38, |v108|
	v_add_f32_e64 v39, v39, |v109|
	v_add_f32_e64 v38, v38, |v110|
	v_add_f32_e32 v28, v38, v39
	v_mfma_f32_32x32x16_f16 v[96:111], v[32:35], v[88:91], 0
	v_add_f32_e64 v38, |v112|, |v113|
	v_add_f32_e64 v39, |v114|, |v115|
	v_add_f32_e64 v38, v38, |v116|
	v_add_f32_e64 v39, v39, |v117|
	v_add_f32_e64 v38, v38, |v118|
	v_add_f32_e64 v39, v39, |v119|
	v_add_f32_e64 v38, v38, |v120|
	v_add_f32_e64 v39, v39, |v121|
	v_add_f32_e64 v38, v38, |v122|
	v_add_f32_e64 v39, v39, |v123|
	v_add_f32_e64 v38, v38, |v124|
	v_add_f32_e64 v39, v39, |v125|
	v_add_f32_e64 v38, v38, |v126|
	v_add_f32_e32 v29, v38, v39
	v_mfma_f32_32x32x16_f16 v[112:127], v[32:35], v[92:95], 0
	v_add_f32_e64 v38, |v96|, |v97|
	v_add_f32_e64 v39, |v98|, |v99|
	v_add_f32_e64 v38, v38, |v100|
	v_add_f32_e64 v39, v39, |v101|
	v_add_f32_e64 v38, v38, |v102|
	v_add_f32_e64 v39, v39, |v103|
	v_add_f32_e64 v38, v38, |v104|
	v_add_f32_e64 v39, v39, |v105|
	v_add_f32_e64 v38, v38, |v106|
	v_add_f32_e64 v39, v39, |v107|
	v_add_f32_e64 v38, v38, |v108|
	v_add_f32_e64 v39, v39, |v109|
	v_add_f32_e64 v38, v38, |v110|
	v_add_f32_e32 v30, v38, v39
	v_add_f32_e64 v38, |v112|, |v113|
	v_add_f32_e64 v39, |v114|, |v115|
	v_add_f32_e64 v38, v38, |v116|
	v_add_f32_e64 v39, v39, |v117|
	v_add_f32_e64 v38, v38, |v118|
	v_add_f32_e64 v39, v39, |v119|
	v_add_f32_e64 v38, v38, |v120|
	v_add_f32_e64 v39, v39, |v121|
	v_add_f32_e64 v38, v38, |v122|
	v_add_f32_e64 v39, v39, |v123|
	v_add_f32_e64 v38, v38, |v124|
	v_add_f32_e64 v39, v39, |v125|
	v_add_f32_e64 v38, v38, |v126|
	v_add_f32_e32 v31, v38, v39
	s_branch .Lafter_first
.Lf16:
	s_setprio 0
	v_add_f32_e64 v38, |v96|, |v97|
	v_add_f32_e64 v39, |v98|, |v99|
	v_add_f32_e64 v38, v38, |v100|
	v_add_f32_e64 v39, v39, |v101|
	v_add_f32_e64 v38, v38, |v102|
	v_add_f32_e64 v39, v39, |v103|
	v_add_f32_e64 v38, v38, |v104|
	v_add_f32_e64 v39, v39, |v105|
	v_add_f32_e64 v38, v38, |v106|
	v_add_f32_e64 v39, v39, |v107|
	v_add_f32_e64 v38, v38, |v108|
	v_add_f32_e64 v39, v39, |v109|
	v_add_f32_e64 v38, v38, |v110|
	v_add_f32_e64 v39, v39, |v111|
	v_add_f32_e32 v24, v38, v39
	v_mfma_f32_32x32x16_f16 v[96:111], v[32:35], v[72:75], 0
	v_add_f32_e64 v38, |v112|, |v113|
	v_add_f32_e64 v39, |v114|, |v115|
	v_add_f32_e64 v38, v38, |v116|
	v_add_f32_e64 v39, v39, |v117|
	v_add_f32_e64 v38, v38, |v118|
	v_add_f32_e64 v39, v39, |v119|
	v_add_f32_e64 v38, v38, |v120|
	v_add_f32_e64 v39, v39, |v121|
	v_add_f32_e64 v38, v38, |v122|
	v_add_f32_e64 v39, v39, |v123|
	v_add_f32_e64 v38, v38, |v124|
	v_add_f32_e64 v39, v39, |v125|
	v_add_f32_e64 v38, v38, |v126|
	v_add_f32_e64 v39, v39, |v127|
	v_add_f32_e32 v25, v38, v39
	v_mfma_f32_32x32x16_f16 v[112:127], v[32:35], v[76:79], 0
	v_add_f32_e64 v38, |v96|, |v97|
	v_add_f32_e64 v39, |v98|, |v99|
	v_add_f32_e64 v38, v38, |v100|
	v_add_f32_e64 v39, v39, |v101|
	v_add_f32_e64 v38, v38, |v102|
	v_add_f32_e64 v39, v39, |v103|
	v_add_f32_e64 v38, v38, |v104|
	v_add_f32_e64 v39, v39, |v105|
	v_add_f32_e64 v38, v38, |v106|
	v_add_f32_e64 v39, v39, |v107|
	v_add_f32_e64 v38, v38, |v108|
	v_add_f32_e64 v39, v39, |v109|
	v_add_f32_e64 v38, v38, |v110|
	v_add_f32_e64 v39, v39, |v111|
	v_add_f32_e32 v26, v38, v39
	v_mfma_f32_32x32x16_f16 v[96:111], v[32:35], v[80:83], 0
	v_add_f32_e64 v38, |v112|, |v113|
	v_add_f32_e64 v39, |v114|, |v115|
	v_add_f32_e64 v38, v38, |v116|
	v_add_f32_e64 v39, v39, |v117|
	v_add_f32_e64 v38, v38, |v118|
	v_add_f32_e64 v39, v39, |v119|
	v_add_f32_e64 v38, v38, |v120|
	v_add_f32_e64 v39, v39, |v121|
	v_add_f32_e64 v38, v38, |v122|
	v_add_f32_e64 v39, v39, |v123|
	v_add_f32_e64 v38, v38, |v124|
	v_add_f32_e64 v39, v39, |v125|
	v_add_f32_e64 v38, v38, |v126|
	v_add_f32_e64 v39, v39, |v127|
	v_add_f32_e32 v27, v38, v39
	v_mfma_f32_32x32x16_f16 v[112:127], v[32:35], v[84:87], 0
	v_add_f32_e64 v38, |v96|, |v97|
	v_add_f32_e64 v39, |v98|, |v99|
	v_add_f32_e64 v38, v38, |v100|
	v_add_f32_e64 v39, v39, |v101|
	v_add_f32_e64 v38, v38, |v102|
	v_add_f32_e64 v39, v39, |v103|
	v_add_f32_e64 v38, v38, |v104|
	v_add_f32_e64 v39, v39, |v105|
	v_add_f32_e64 v38, v38, |v106|
	v_add_f32_e64 v39, v39, |v107|
	v_add_f32_e64 v38, v38, |v108|
	v_add_f32_e64 v39, v39, |v109|
	v_add_f32_e64 v38, v38, |v110|
	v_add_f32_e64 v39, v39, |v111|
	v_add_f32_e32 v28, v38, v39
	v_mfma_f32_32x32x16_f16 v[96:111], v[32:35], v[88:91], 0
	v_add_f32_e64 v38, |v112|, |v113|
	v_add_f32_e64 v39, |v114|, |v115|
	v_add_f32_e64 v38, v38, |v116|
	v_add_f32_e64 v39, v39, |v117|
	v_add_f32_e64 v38, v38, |v118|
	v_add_f32_e64 v39, v39, |v119|
	v_add_f32_e64 v38, v38, |v120|
	v_add_f32_e64 v39, v39, |v121|
	v_add_f32_e64 v38, v38, |v122|
	v_add_f32_e64 v39, v39, |v123|
	v_add_f32_e64 v38, v38, |v124|
	v_add_f32_e64 v39, v39, |v125|
	v_add_f32_e64 v38, v38, |v126|
	v_add_f32_e64 v39, v39, |v127|
	v_add_f32_e32 v29, v38, v39
	v_mfma_f32_32x32x16_f16 v[112:127], v[32:35], v[92:95], 0
	v_add_f32_e64 v38, |v96|, |v97|
	v_add_f32_e64 v39, |v98|, |v99|
	v_add_f32_e64 v38, v38, |v100|
	v_add_f32_e64 v39, v39, |v101|
	v_add_f32_e64 v38, v38, |v102|
	v_add_f32_e64 v39, v39, |v103|
	v_add_f32_e64 v38, v38, |v104|
	v_add_f32_e64 v39, v39, |v105|
	v_add_f32_e64 v38, v38, |v106|
	v_add_f32_e64 v39, v39, |v107|
	v_add_f32_e64 v38, v38, |v108|
	v_add_f32_e64 v39, v39, |v109|
	v_add_f32_e64 v38, v38, |v110|
	v_add_f32_e64 v39, v39, |v111|
	v_add_f32_e32 v30, v38, v39
	v_add_f32_e64 v38, |v112|, |v113|
	v_add_f32_e64 v39, |v114|, |v115|
	v_add_f32_e64 v38, v38, |v116|
	v_add_f32_e64 v39, v39, |v117|
	v_add_f32_e64 v38, v38, |v118|
	v_add_f32_e64 v39, v39, |v119|
	v_add_f32_e64 v38, v38, |v120|
	v_add_f32_e64 v39, v39, |v121|
	v_add_f32_e64 v38, v38, |v122|
	v_add_f32_e64 v39, v39, |v123|
	v_add_f32_e64 v38, v38, |v124|
	v_add_f32_e64 v39, v39, |v125|
	v_add_f32_e64 v38, v38, |v126|
	v_add_f32_e64 v39, v39, |v127|
	v_add_f32_e32 v31, v38, v39
